# speedup vs baseline: 1.0108x; 1.0043x over previous
.Lh_no_out:
	s_cmp_eq_u32 s17, 0
	s_cselect_b32 s4, s4, s6
	s_cselect_b32 s5, s5, s7
	s_add_u32 s24, s8, s22
	s_addc_u32 s25, s9, 0
	s_add_u32 s4, s4, s21
	s_addc_u32 s5, s5, 0
	global_load_dwordx4 v[14:17], v18, s[24:25] nt
	global_load_dwordx4 v[2:5], v18, s[4:5] nt
	s_add_u32 s6, s4, 0x40000
	s_addc_u32 s7, s5, 0
	s_add_u32 s8, s4, 0x80000
	s_addc_u32 s9, s5, 0
	s_barrier
	global_load_dwordx4 v[6:9], v18, s[6:7] nt
	s_barrier
	global_load_dwordx4 v[10:13], v18, s[8:9] nt
	s_cmp_gt_u32 s3, 11
	s_cbranch_scc1 .Lh_nowarm
	s_getpc_b64 s[60:61]
.Lh_pc:
	s_add_u32 s60, s60, _Z7k_finalPKfPKiPf-.Lh_pc
	s_addc_u32 s61, s61, 0
	s_lshl_b32 s62, s3, 7
	s_add_u32 s60, s60, s62
	s_addc_u32 s61, s61, 0
	s_load_dwordx16 s[64:79], s[60:61], 0x0
	s_load_dwordx16 s[64:79], s[60:61], 0x40
.Lh_nowarm:
	s_mul_i32 s46, s3, 0xc00
	s_add_u32 s46, s46, 0x8420
	v_lshl_add_u32 v26, v1, 2, s46
	v_and_b32_e32 v38, 15, v0
	s_mul_i32 s58, s17, 0x4200
	s_add_u32 s58, s58, 0x1e0
	v_lshl_add_u32 v38, v38, 2, s58
	v_add_u32_e32 v39, 0x1600, v38
	v_add_u32_e32 v40, 0x2c00, v38
	v_mov_b32_e32 v41, 0x41fc0000
	v_mov_b32_e32 v42, 0xbf38aa3b
	s_mov_b32 s48, 0x3f940000
	s_mov_b32 s51, 0x3fb8aa3b
	s_mov_b32 s42, 0
	s_mov_b32 s43, 0
	s_mov_b32 s44, 0x7fffffff
	s_mov_b32 s45, 0x7fffffff
	s_mov_b32 s47, 0
	s_mul_i32 s58, s3, 0x1600
	s_add_u32 s58, s58, 0x320
	v_lshl_add_u32 v44, v1, 6, s58
	v_bfe_u32 v45, v1, 2, 2
	v_lshlrev_b32_e32 v45, 4, v45
	v_xor_b32_e32 v46, 16, v45
	v_xor_b32_e32 v47, 32, v45
	v_xor_b32_e32 v48, 48, v45
	v_add_u32_e32 v45, v44, v45
	v_add_u32_e32 v46, v44, v46
	v_add_u32_e32 v47, v44, v47
	v_add_u32_e32 v48, v44, v48
	s_mul_i32 s58, s2, 0x600
	s_lshl_b32 s59, s3, 8
	s_add_u32 s58, s58, s59
	s_add_u32 s10, s10, s58
	s_addc_u32 s11, s11, 0
	v_lshlrev_b32_e32 v49, 2, v1
	s_lshl_b32 s58, s2, 2
	s_add_u32 s12, s12, s58
	s_addc_u32 s13, s13, 0
	s_setprio 3
	s_cmp_lt_u32 s3, 8
	s_cbranch_scc1 .Lh_nostagger
	s_sleep 3

	.amdhsa_kernel _Z6k_histPKfS0_S0_PfPiS1_
		.amdhsa_group_segment_fixed_size 32
		.amdhsa_private_segment_fixed_size 0
		.amdhsa_kernarg_size 48
		.amdhsa_user_sgpr_count 2
		.amdhsa_user_sgpr_dispatch_ptr 0
		.amdhsa_user_sgpr_queue_ptr 0
		.amdhsa_user_sgpr_kernarg_segment_ptr 1
		.amdhsa_user_sgpr_dispatch_id 0
		.amdhsa_user_sgpr_kernarg_preload_length 0
		.amdhsa_user_sgpr_kernarg_preload_offset 0
		.amdhsa_user_sgpr_private_segment_size 0
		.amdhsa_uses_dynamic_stack 0
		.amdhsa_enable_private_segment 0
		.amdhsa_system_sgpr_workgroup_id_x 1
		.amdhsa_system_sgpr_workgroup_id_y 0
		.amdhsa_system_sgpr_workgroup_id_z 0
		.amdhsa_system_sgpr_workgroup_info 0
		.amdhsa_system_vgpr_workitem_id 0
		.amdhsa_next_free_vgpr 50
		.amdhsa_next_free_sgpr 80
		.amdhsa_accum_offset 52
		.amdhsa_reserve_vcc 1
		.amdhsa_float_round_mode_32 0
		.amdhsa_float_round_mode_16_64 0
		.amdhsa_float_denorm_mode_32 3
		.amdhsa_float_denorm_mode_16_64 3
		.amdhsa_dx10_clamp 1
		.amdhsa_ieee_mode 1
		.amdhsa_fp16_overflow 0
		.amdhsa_tg_split 0
		.amdhsa_exception_fp_ieee_invalid_op 0
		.amdhsa_exception_fp_denorm_src 0
		.amdhsa_exception_fp_ieee_div_zero 0
		.amdhsa_exception_fp_ieee_overflow 0
		.amdhsa_exception_fp_ieee_underflow 0
		.amdhsa_exception_fp_ieee_inexact 0
		.amdhsa_exception_int_div_zero 0
	.end_amdhsa_kernel

.Lfunc_end0:
	.size	_Z6k_histPKfS0_S0_PfPiS1_, .Lfunc_end0-_Z6k_histPKfS0_S0_PfPiS1_
	.set _Z6k_histPKfS0_S0_PfPiS1_.num_vgpr, 50
	.set _Z6k_histPKfS0_S0_PfPiS1_.num_agpr, 0
	.set _Z6k_histPKfS0_S0_PfPiS1_.numbered_sgpr, 80
	.set _Z6k_histPKfS0_S0_PfPiS1_.num_named_barrier, 0
	.set _Z6k_histPKfS0_S0_PfPiS1_.private_seg_size, 0
	.set _Z6k_histPKfS0_S0_PfPiS1_.uses_vcc, 1
	.set _Z6k_histPKfS0_S0_PfPiS1_.uses_flat_scratch, 0
	.set _Z6k_histPKfS0_S0_PfPiS1_.has_dyn_sized_stack, 0
	.set _Z6k_histPKfS0_S0_PfPiS1_.has_recursion, 0
	.set _Z6k_histPKfS0_S0_PfPiS1_.has_indirect_call, 0

amdhsa.kernels:
  - .agpr_count:     0
    .args:
      - .actual_access:  read_only
        .address_space:  global
        .offset:         0
        .size:           8
        .value_kind:     global_buffer
      - .actual_access:  read_only
        .address_space:  global
        .offset:         8
        .size:           8
        .value_kind:     global_buffer
      - .actual_access:  read_only
        .address_space:  global
        .offset:         16
        .size:           8
        .value_kind:     global_buffer
      - .actual_access:  write_only
        .address_space:  global
        .offset:         24
        .size:           8
        .value_kind:     global_buffer
      - .actual_access:  write_only
        .address_space:  global
        .offset:         32
        .size:           8
        .value_kind:     global_buffer
      - .actual_access:  write_only
        .address_space:  global
        .offset:         40
        .size:           8
        .value_kind:     global_buffer
    .group_segment_fixed_size: 32
    .kernarg_segment_align: 8
    .kernarg_segment_size: 48
    .language:       OpenCL C
    .language_version:
      - 2
      - 0
    .max_flat_workgroup_size: 1024
    .name:           _Z6k_histPKfS0_S0_PfPiS1_
    .private_segment_fixed_size: 0
    .sgpr_count:     86
    .sgpr_spill_count: 0
    .symbol:         _Z6k_histPKfS0_S0_PfPiS1_.kd
    .uniform_work_group_size: 1
    .uses_dynamic_stack: false
    .vgpr_count:     50
    .vgpr_spill_count: 0
    .wavefront_size: 64
  - .agpr_count:     0
    .args:
      - .actual_access:  read_only
        .address_space:  global
        .offset:         0
        .size:           8
        .value_kind:     global_buffer
      - .actual_access:  read_only
        .address_space:  global
        .offset:         8
        .size:           8
        .value_kind:     global_buffer
      - .address_space:  global
        .offset:         16
        .size:           8
        .value_kind:     global_buffer
    .group_segment_fixed_size: 2080
    .kernarg_segment_align: 8
    .kernarg_segment_size: 24
    .language:       OpenCL C
    .language_version:
      - 2
      - 0
    .max_flat_workgroup_size: 256
    .name:           _Z7k_finalPKfPKiPf
    .private_segment_fixed_size: 0
    .sgpr_count:     34
    .sgpr_spill_count: 0
    .symbol:         _Z7k_finalPKfPKiPf.kd
    .uniform_work_group_size: 1
    .uses_dynamic_stack: false
    .vgpr_count:     36
    .vgpr_spill_count: 0
    .wavefront_size: 64
